# baseline (speedup 1.0000x reference)
.LBB1_40:
	v_add_u32_e32 v2, s0, v18
	v_and_b32_e32 v20, 32, v19
	v_ashrrev_i32_e32 v21, 8, v19
	v_and_b32_e32 v22, 0x7c0, v16
	v_add_u32_e32 v23, s0, v14
	v_lshrrev_b32_e32 v34, 7, v2
	v_bitop3_b32 v20, v2, v20, 48 bitop3:0x6c
	v_and_b32_e32 v24, 32, v15
	v_ashrrev_i32_e32 v25, 8, v15
	v_lshrrev_b32_e32 v35, 5, v2
	v_lshrrev_b32_e32 v36, 9, v2
	v_bfe_u32 v37, v2, 6, 2
	v_and_b32_e32 v21, 0xffffff80, v21
	v_lshlrev_b32_e32 v2, 2, v22
	v_lshrrev_b32_e32 v22, 7, v23
	v_lshrrev_b32_e32 v20, 1, v20
	v_and_b32_e32 v34, 0x60, v34
	v_add_u32_e32 v26, s0, v10
	v_lshrrev_b32_e32 v38, 5, v23
	v_bitop3_b32 v24, v23, v24, 48 bitop3:0x6c
	v_lshrrev_b32_e32 v39, 9, v23
	v_bfe_u32 v23, v23, 6, 2
	v_and_b32_e32 v25, 0xffffff80, v25
	v_and_b32_e32 v47, 24, v35
	v_and_b32_e32 v36, 4, v36
	v_and_b32_e32 v22, 0x60, v22
	v_and_or_b32 v35, v35, 32, v20
	v_or3_b32 v20, v37, v21, v34
	v_and_b32_e32 v27, 32, v11
	v_ashrrev_i32_e32 v28, 8, v11
	v_lshrrev_b32_e32 v41, 7, v26
	v_and_b32_e32 v48, 24, v38
	v_and_b32_e32 v39, 4, v39
	v_or3_b32 v21, v23, v25, v22
	v_or3_b32 v20, v20, v36, v47
	v_add_u32_e32 v29, s0, v6
	v_lshrrev_b32_e32 v42, 5, v26
	v_bitop3_b32 v27, v26, v27, 48 bitop3:0x6c
	v_lshrrev_b32_e32 v43, 9, v26
	v_bfe_u32 v26, v26, 6, 2
	v_and_b32_e32 v28, 0xffffff80, v28
	v_and_b32_e32 v41, 0x60, v41
	v_or3_b32 v22, v21, v39, v48
	v_ashrrev_i32_e32 v21, 31, v20
	v_and_b32_e32 v30, 32, v7
	v_ashrrev_i32_e32 v31, 8, v7
	v_lshrrev_b32_e32 v44, 7, v29
	v_lshrrev_b32_e32 v24, 1, v24
	v_and_b32_e32 v49, 24, v42
	v_and_b32_e32 v43, 4, v43
	v_or3_b32 v23, v26, v28, v41
	v_lshlrev_b64 v[20:21], 13, v[20:21]
	v_lshrrev_b32_e32 v45, 5, v29
	v_bitop3_b32 v30, v29, v30, 48 bitop3:0x6c
	v_lshrrev_b32_e32 v46, 9, v29
	v_bfe_u32 v29, v29, 6, 2
	v_and_b32_e32 v31, 0xffffff80, v31
	v_and_b32_e32 v44, 0x60, v44
	v_and_or_b32 v34, v38, 32, v24
	v_or3_b32 v24, v23, v43, v49
	v_ashrrev_i32_e32 v23, 31, v22
	v_lshl_add_u64 v[20:21], s[38:39], 0, v[20:21]
	v_and_b32_e32 v32, 0x7c0, v12
	v_lshrrev_b32_e32 v30, 1, v30
	v_and_b32_e32 v50, 24, v45
	v_and_b32_e32 v46, 4, v46
	v_or3_b32 v25, v29, v31, v44
	v_lshlrev_b64 v[22:23], 13, v[22:23]
	v_lshl_add_u64 v[20:21], v[20:21], 0, v[2:3]
	v_lshlrev_b32_e32 v2, 2, v35
	v_and_or_b32 v51, v45, 32, v30
	v_or3_b32 v26, v25, v46, v50
	v_ashrrev_i32_e32 v25, 31, v24
	v_lshl_add_u64 v[28:29], s[38:39], 0, v[22:23]
	v_lshl_add_u64 v[30:31], v[20:21], 0, v[2:3]
	v_lshlrev_b32_e32 v2, 2, v32
	v_and_b32_e32 v33, 0x7c0, v8
	v_lshrrev_b32_e32 v27, 1, v27
	v_lshlrev_b64 v[24:25], 13, v[24:25]
	v_lshl_add_u64 v[28:29], v[28:29], 0, v[2:3]
	v_lshlrev_b32_e32 v2, 2, v34
	v_and_or_b32 v42, v42, 32, v27
	v_ashrrev_i32_e32 v27, 31, v26
	v_lshl_add_u64 v[36:37], s[38:39], 0, v[24:25]
	v_lshl_add_u64 v[38:39], v[28:29], 0, v[2:3]
	v_lshlrev_b32_e32 v2, 2, v33
	v_and_b32_e32 v40, 0x7c0, v0
	v_lshlrev_b64 v[26:27], 13, v[26:27]
	v_lshl_add_u64 v[36:37], v[36:37], 0, v[2:3]
	v_lshlrev_b32_e32 v2, 2, v42
	v_lshl_add_u64 v[44:45], s[38:39], 0, v[26:27]
	global_load_dwordx4 v[20:23], v[30:31], off nt
	global_load_dwordx4 v[24:27], v[30:31], off offset:16 nt
	v_lshl_add_u64 v[46:47], v[36:37], 0, v[2:3]
	v_lshlrev_b32_e32 v2, 2, v40
	global_load_dwordx4 v[28:31], v[38:39], off offset:16 nt
	global_load_dwordx4 v[32:35], v[38:39], off nt
	v_lshl_add_u64 v[44:45], v[44:45], 0, v[2:3]
	v_lshlrev_b32_e32 v2, 2, v51
	global_load_dwordx4 v[36:39], v[46:47], off nt
	global_load_dwordx4 v[40:43], v[46:47], off offset:16 nt
	v_lshl_add_u64 v[52:53], v[44:45], 0, v[2:3]
	global_load_dwordx4 v[44:47], v[52:53], off nt
	global_load_dwordx4 v[48:51], v[52:53], off offset:16 nt
	v_lshl_add_u64 v[52:53], v[4:5], 0, s[0:1]
	v_add_co_u32_e32 v54, vcc, s4, v52
	s_add_u32 s0, s0, 0x8000
	s_nop 0
	v_addc_co_u32_e32 v55, vcc, 0, v53, vcc
	v_add_co_u32_e32 v56, vcc, s5, v52
	s_addc_u32 s1, s1, 0
	s_nop 0
	v_addc_co_u32_e32 v57, vcc, 0, v53, vcc
	v_add_co_u32_e32 v58, vcc, s6, v52
	v_lshl_add_u64 v[0:1], v[0:1], 0, s[2:3]
	v_add_u32_e32 v7, 0x800, v7
	v_lshl_add_u64 v[8:9], v[8:9], 0, s[2:3]
	v_add_u32_e32 v11, 0x800, v11
	v_lshl_add_u64 v[12:13], v[12:13], 0, s[2:3]
	v_add_u32_e32 v15, 0x800, v15
	v_lshl_add_u64 v[16:17], v[16:17], 0, s[2:3]
	v_add_u32_e32 v19, 0x800, v19
	v_addc_co_u32_e32 v59, vcc, 0, v53, vcc
	v_add_u32_e32 v2, s0, v18
	v_and_b32_e32 v60, 32, v19
	v_ashrrev_i32_e32 v61, 8, v19
	v_and_b32_e32 v62, 0x7c0, v16
	v_add_u32_e32 v63, s0, v14
	v_lshrrev_b32_e32 v74, 7, v2
	v_bitop3_b32 v60, v2, v60, 48 bitop3:0x6c
	v_and_b32_e32 v64, 32, v15
	v_ashrrev_i32_e32 v65, 8, v15
	v_lshrrev_b32_e32 v75, 5, v2
	v_lshrrev_b32_e32 v76, 9, v2
	v_bfe_u32 v77, v2, 6, 2
	v_and_b32_e32 v61, 0xffffff80, v61
	v_lshlrev_b32_e32 v2, 2, v62
	v_lshrrev_b32_e32 v62, 7, v63
	v_lshrrev_b32_e32 v60, 1, v60
	v_and_b32_e32 v74, 0x60, v74
	v_add_u32_e32 v66, s0, v10
	v_lshrrev_b32_e32 v78, 5, v63
	v_bitop3_b32 v64, v63, v64, 48 bitop3:0x6c
	v_lshrrev_b32_e32 v79, 9, v63
	v_bfe_u32 v63, v63, 6, 2
	v_and_b32_e32 v65, 0xffffff80, v65
	v_and_b32_e32 v87, 24, v75
	v_and_b32_e32 v76, 4, v76
	v_and_b32_e32 v62, 0x60, v62
	v_and_or_b32 v75, v75, 32, v60
	v_or3_b32 v60, v77, v61, v74
	v_and_b32_e32 v67, 32, v11
	v_ashrrev_i32_e32 v68, 8, v11
	v_lshrrev_b32_e32 v81, 7, v66
	v_and_b32_e32 v88, 24, v78
	v_and_b32_e32 v79, 4, v79
	v_or3_b32 v61, v63, v65, v62
	v_or3_b32 v60, v60, v76, v87
	v_add_u32_e32 v69, s0, v6
	v_lshrrev_b32_e32 v82, 5, v66
	v_bitop3_b32 v67, v66, v67, 48 bitop3:0x6c
	v_lshrrev_b32_e32 v83, 9, v66
	v_bfe_u32 v66, v66, 6, 2
	v_and_b32_e32 v68, 0xffffff80, v68
	v_and_b32_e32 v81, 0x60, v81
	v_or3_b32 v62, v61, v79, v88
	v_ashrrev_i32_e32 v61, 31, v60
	v_and_b32_e32 v70, 32, v7
	v_ashrrev_i32_e32 v71, 8, v7
	v_lshrrev_b32_e32 v84, 7, v69
	v_lshrrev_b32_e32 v64, 1, v64
	v_and_b32_e32 v89, 24, v82
	v_and_b32_e32 v83, 4, v83
	v_or3_b32 v63, v66, v68, v81
	v_lshlrev_b64 v[60:61], 13, v[60:61]
	v_lshrrev_b32_e32 v85, 5, v69
	v_bitop3_b32 v70, v69, v70, 48 bitop3:0x6c
	v_lshrrev_b32_e32 v86, 9, v69
	v_bfe_u32 v69, v69, 6, 2
	v_and_b32_e32 v71, 0xffffff80, v71
	v_and_b32_e32 v84, 0x60, v84
	v_and_or_b32 v74, v78, 32, v64
	v_or3_b32 v64, v63, v83, v89
	v_ashrrev_i32_e32 v63, 31, v62
	v_lshl_add_u64 v[60:61], s[38:39], 0, v[60:61]
	v_and_b32_e32 v72, 0x7c0, v12
	v_lshrrev_b32_e32 v70, 1, v70
	v_and_b32_e32 v90, 24, v85
	v_and_b32_e32 v86, 4, v86
	v_or3_b32 v65, v69, v71, v84
	v_lshlrev_b64 v[62:63], 13, v[62:63]
	v_lshl_add_u64 v[60:61], v[60:61], 0, v[2:3]
	v_lshlrev_b32_e32 v2, 2, v75
	v_and_or_b32 v91, v85, 32, v70
	v_or3_b32 v66, v65, v86, v90
	v_ashrrev_i32_e32 v65, 31, v64
	v_lshl_add_u64 v[68:69], s[38:39], 0, v[62:63]
	v_lshl_add_u64 v[70:71], v[60:61], 0, v[2:3]
	v_lshlrev_b32_e32 v2, 2, v72
	v_and_b32_e32 v73, 0x7c0, v8
	v_lshrrev_b32_e32 v67, 1, v67
	v_lshlrev_b64 v[64:65], 13, v[64:65]
	v_lshl_add_u64 v[68:69], v[68:69], 0, v[2:3]
	v_lshlrev_b32_e32 v2, 2, v74
	v_and_or_b32 v82, v82, 32, v67
	v_ashrrev_i32_e32 v67, 31, v66
	v_lshl_add_u64 v[76:77], s[38:39], 0, v[64:65]
	v_lshl_add_u64 v[78:79], v[68:69], 0, v[2:3]
	v_lshlrev_b32_e32 v2, 2, v73
	v_and_b32_e32 v80, 0x7c0, v0
	v_lshlrev_b64 v[66:67], 13, v[66:67]
	v_lshl_add_u64 v[76:77], v[76:77], 0, v[2:3]
	v_lshlrev_b32_e32 v2, 2, v82
	v_lshl_add_u64 v[84:85], s[38:39], 0, v[66:67]
	global_load_dwordx4 v[60:63], v[70:71], off nt
	global_load_dwordx4 v[64:67], v[70:71], off offset:16 nt
	v_lshl_add_u64 v[86:87], v[76:77], 0, v[2:3]
	v_lshlrev_b32_e32 v2, 2, v80
	global_load_dwordx4 v[68:71], v[78:79], off offset:16 nt
	global_load_dwordx4 v[72:75], v[78:79], off nt
	v_lshl_add_u64 v[84:85], v[84:85], 0, v[2:3]
	v_lshlrev_b32_e32 v2, 2, v91
	global_load_dwordx4 v[76:79], v[86:87], off nt
	global_load_dwordx4 v[80:83], v[86:87], off offset:16 nt
	v_lshl_add_u64 v[92:93], v[84:85], 0, v[2:3]
	global_load_dwordx4 v[84:87], v[92:93], off nt
	global_load_dwordx4 v[88:91], v[92:93], off offset:16 nt
	v_lshl_add_u64 v[92:93], v[4:5], 0, s[0:1]
	v_add_co_u32_e32 v94, vcc, s4, v92
	s_add_u32 s0, s0, 0x8000
	s_nop 0
	v_addc_co_u32_e32 v95, vcc, 0, v93, vcc
	v_add_co_u32_e32 v96, vcc, s5, v92
	s_addc_u32 s1, s1, 0
	s_nop 0
	v_addc_co_u32_e32 v97, vcc, 0, v93, vcc
	v_add_co_u32_e32 v98, vcc, s6, v92
	v_lshl_add_u64 v[0:1], v[0:1], 0, s[2:3]
	v_add_u32_e32 v7, 0x800, v7
	v_lshl_add_u64 v[8:9], v[8:9], 0, s[2:3]
	v_add_u32_e32 v11, 0x800, v11
	v_lshl_add_u64 v[12:13], v[12:13], 0, s[2:3]
	v_add_u32_e32 v15, 0x800, v15
	v_lshl_add_u64 v[16:17], v[16:17], 0, s[2:3]
	v_add_u32_e32 v19, 0x800, v19
	v_addc_co_u32_e32 v99, vcc, 0, v93, vcc
	v_add_u32_e32 v2, s0, v18
	v_and_b32_e32 v100, 32, v19
	v_ashrrev_i32_e32 v101, 8, v19
	v_and_b32_e32 v102, 0x7c0, v16
	v_add_u32_e32 v103, s0, v14
	v_lshrrev_b32_e32 v114, 7, v2
	v_bitop3_b32 v100, v2, v100, 48 bitop3:0x6c
	v_and_b32_e32 v104, 32, v15
	v_ashrrev_i32_e32 v105, 8, v15
	v_lshrrev_b32_e32 v115, 5, v2
	v_lshrrev_b32_e32 v116, 9, v2
	v_bfe_u32 v117, v2, 6, 2
	v_and_b32_e32 v101, 0xffffff80, v101
	v_lshlrev_b32_e32 v2, 2, v102
	v_lshrrev_b32_e32 v102, 7, v103
	v_lshrrev_b32_e32 v100, 1, v100
	v_and_b32_e32 v114, 0x60, v114
	v_add_u32_e32 v106, s0, v10
	v_lshrrev_b32_e32 v118, 5, v103
	v_bitop3_b32 v104, v103, v104, 48 bitop3:0x6c
	v_lshrrev_b32_e32 v119, 9, v103
	v_bfe_u32 v103, v103, 6, 2
	v_and_b32_e32 v105, 0xffffff80, v105
	v_and_b32_e32 v127, 24, v115
	v_and_b32_e32 v116, 4, v116
	v_and_b32_e32 v102, 0x60, v102
	v_and_or_b32 v115, v115, 32, v100
	v_or3_b32 v100, v117, v101, v114
	v_and_b32_e32 v107, 32, v11
	v_ashrrev_i32_e32 v108, 8, v11
	v_lshrrev_b32_e32 v121, 7, v106
	v_and_b32_e32 v128, 24, v118
	v_and_b32_e32 v119, 4, v119
	v_or3_b32 v101, v103, v105, v102
	v_or3_b32 v100, v100, v116, v127
	v_add_u32_e32 v109, s0, v6
	v_lshrrev_b32_e32 v122, 5, v106
	v_bitop3_b32 v107, v106, v107, 48 bitop3:0x6c
	v_lshrrev_b32_e32 v123, 9, v106
	v_bfe_u32 v106, v106, 6, 2
	v_and_b32_e32 v108, 0xffffff80, v108
	v_and_b32_e32 v121, 0x60, v121
	v_or3_b32 v102, v101, v119, v128
	v_ashrrev_i32_e32 v101, 31, v100
	v_and_b32_e32 v110, 32, v7
	v_ashrrev_i32_e32 v111, 8, v7
	v_lshrrev_b32_e32 v124, 7, v109
	v_lshrrev_b32_e32 v104, 1, v104
	v_and_b32_e32 v129, 24, v122
	v_and_b32_e32 v123, 4, v123
	v_or3_b32 v103, v106, v108, v121
	v_lshlrev_b64 v[100:101], 13, v[100:101]
	v_lshrrev_b32_e32 v125, 5, v109
	v_bitop3_b32 v110, v109, v110, 48 bitop3:0x6c
	v_lshrrev_b32_e32 v126, 9, v109
	v_bfe_u32 v109, v109, 6, 2
	v_and_b32_e32 v111, 0xffffff80, v111
	v_and_b32_e32 v124, 0x60, v124
	v_and_or_b32 v114, v118, 32, v104
	v_or3_b32 v104, v103, v123, v129
	v_ashrrev_i32_e32 v103, 31, v102
	v_lshl_add_u64 v[100:101], s[38:39], 0, v[100:101]
	v_and_b32_e32 v112, 0x7c0, v12
	v_lshrrev_b32_e32 v110, 1, v110
	v_and_b32_e32 v130, 24, v125
	v_and_b32_e32 v126, 4, v126
	v_or3_b32 v105, v109, v111, v124
	v_lshlrev_b64 v[102:103], 13, v[102:103]
	v_lshl_add_u64 v[100:101], v[100:101], 0, v[2:3]
	v_lshlrev_b32_e32 v2, 2, v115
	v_and_or_b32 v131, v125, 32, v110
	v_or3_b32 v106, v105, v126, v130
	v_ashrrev_i32_e32 v105, 31, v104
	v_lshl_add_u64 v[108:109], s[38:39], 0, v[102:103]
	v_lshl_add_u64 v[110:111], v[100:101], 0, v[2:3]
	v_lshlrev_b32_e32 v2, 2, v112
	v_and_b32_e32 v113, 0x7c0, v8
	v_lshrrev_b32_e32 v107, 1, v107
	v_lshlrev_b64 v[104:105], 13, v[104:105]
	v_lshl_add_u64 v[108:109], v[108:109], 0, v[2:3]
	v_lshlrev_b32_e32 v2, 2, v114
	v_and_or_b32 v122, v122, 32, v107
	v_ashrrev_i32_e32 v107, 31, v106
	v_lshl_add_u64 v[116:117], s[38:39], 0, v[104:105]
	v_lshl_add_u64 v[118:119], v[108:109], 0, v[2:3]
	v_lshlrev_b32_e32 v2, 2, v113
	v_and_b32_e32 v120, 0x7c0, v0
	v_lshlrev_b64 v[106:107], 13, v[106:107]
	v_lshl_add_u64 v[116:117], v[116:117], 0, v[2:3]
	v_lshlrev_b32_e32 v2, 2, v122
	v_lshl_add_u64 v[124:125], s[38:39], 0, v[106:107]
	global_load_dwordx4 v[100:103], v[110:111], off nt
	global_load_dwordx4 v[104:107], v[110:111], off offset:16 nt
	v_lshl_add_u64 v[126:127], v[116:117], 0, v[2:3]
	v_lshlrev_b32_e32 v2, 2, v120
	global_load_dwordx4 v[108:111], v[118:119], off offset:16 nt
	global_load_dwordx4 v[112:115], v[118:119], off nt
	v_lshl_add_u64 v[124:125], v[124:125], 0, v[2:3]
	v_lshlrev_b32_e32 v2, 2, v131
	global_load_dwordx4 v[116:119], v[126:127], off nt
	global_load_dwordx4 v[120:123], v[126:127], off offset:16 nt
	v_lshl_add_u64 v[132:133], v[124:125], 0, v[2:3]
	global_load_dwordx4 v[124:127], v[132:133], off nt
	global_load_dwordx4 v[128:131], v[132:133], off offset:16 nt
	v_lshl_add_u64 v[132:133], v[4:5], 0, s[0:1]
	v_add_co_u32_e32 v134, vcc, s4, v132
	s_add_u32 s0, s0, 0x8000
	s_nop 0
	v_addc_co_u32_e32 v135, vcc, 0, v133, vcc
	v_add_co_u32_e32 v136, vcc, s5, v132
	s_addc_u32 s1, s1, 0
	s_nop 0
	v_addc_co_u32_e32 v137, vcc, 0, v133, vcc
	v_add_co_u32_e32 v138, vcc, s6, v132
	v_lshl_add_u64 v[0:1], v[0:1], 0, s[2:3]
	v_add_u32_e32 v7, 0x800, v7
	v_lshl_add_u64 v[8:9], v[8:9], 0, s[2:3]
	v_add_u32_e32 v11, 0x800, v11
	v_lshl_add_u64 v[12:13], v[12:13], 0, s[2:3]
	v_add_u32_e32 v15, 0x800, v15
	v_lshl_add_u64 v[16:17], v[16:17], 0, s[2:3]
	v_add_u32_e32 v19, 0x800, v19
	v_addc_co_u32_e32 v139, vcc, 0, v133, vcc
	v_add_u32_e32 v2, s0, v18
	v_and_b32_e32 v140, 32, v19
	v_ashrrev_i32_e32 v141, 8, v19
	v_and_b32_e32 v142, 0x7c0, v16
	v_add_u32_e32 v143, s0, v14
	v_lshrrev_b32_e32 v154, 7, v2
	v_bitop3_b32 v140, v2, v140, 48 bitop3:0x6c
	v_and_b32_e32 v144, 32, v15
	v_ashrrev_i32_e32 v145, 8, v15
	v_lshrrev_b32_e32 v155, 5, v2
	v_lshrrev_b32_e32 v156, 9, v2
	v_bfe_u32 v157, v2, 6, 2
	v_and_b32_e32 v141, 0xffffff80, v141
	v_lshlrev_b32_e32 v2, 2, v142
	v_lshrrev_b32_e32 v142, 7, v143
	v_lshrrev_b32_e32 v140, 1, v140
	v_and_b32_e32 v154, 0x60, v154
	v_add_u32_e32 v146, s0, v10
	v_lshrrev_b32_e32 v158, 5, v143
	v_bitop3_b32 v144, v143, v144, 48 bitop3:0x6c
	v_lshrrev_b32_e32 v159, 9, v143
	v_bfe_u32 v143, v143, 6, 2
	v_and_b32_e32 v145, 0xffffff80, v145
	v_and_b32_e32 v167, 24, v155
	v_and_b32_e32 v156, 4, v156
	v_and_b32_e32 v142, 0x60, v142
	v_and_or_b32 v155, v155, 32, v140
	v_or3_b32 v140, v157, v141, v154
	v_and_b32_e32 v147, 32, v11
	v_ashrrev_i32_e32 v148, 8, v11
	v_lshrrev_b32_e32 v161, 7, v146
	v_and_b32_e32 v168, 24, v158
	v_and_b32_e32 v159, 4, v159
	v_or3_b32 v141, v143, v145, v142
	v_or3_b32 v140, v140, v156, v167
	v_add_u32_e32 v149, s0, v6
	v_lshrrev_b32_e32 v162, 5, v146
	v_bitop3_b32 v147, v146, v147, 48 bitop3:0x6c
	v_lshrrev_b32_e32 v163, 9, v146
	v_bfe_u32 v146, v146, 6, 2
	v_and_b32_e32 v148, 0xffffff80, v148
	v_and_b32_e32 v161, 0x60, v161
	v_or3_b32 v142, v141, v159, v168
	v_ashrrev_i32_e32 v141, 31, v140
	v_and_b32_e32 v150, 32, v7
	v_ashrrev_i32_e32 v151, 8, v7
	v_lshrrev_b32_e32 v164, 7, v149
	v_lshrrev_b32_e32 v144, 1, v144
	v_and_b32_e32 v169, 24, v162
	v_and_b32_e32 v163, 4, v163
	v_or3_b32 v143, v146, v148, v161
	v_lshlrev_b64 v[140:141], 13, v[140:141]
	v_lshrrev_b32_e32 v165, 5, v149
	v_bitop3_b32 v150, v149, v150, 48 bitop3:0x6c
	v_lshrrev_b32_e32 v166, 9, v149
	v_bfe_u32 v149, v149, 6, 2
	v_and_b32_e32 v151, 0xffffff80, v151
	v_and_b32_e32 v164, 0x60, v164
	v_and_or_b32 v154, v158, 32, v144
	v_or3_b32 v144, v143, v163, v169
	v_ashrrev_i32_e32 v143, 31, v142
	v_lshl_add_u64 v[140:141], s[38:39], 0, v[140:141]
	v_and_b32_e32 v152, 0x7c0, v12
	v_lshrrev_b32_e32 v150, 1, v150
	v_and_b32_e32 v170, 24, v165
	v_and_b32_e32 v166, 4, v166
	v_or3_b32 v145, v149, v151, v164
	v_lshlrev_b64 v[142:143], 13, v[142:143]
	v_lshl_add_u64 v[140:141], v[140:141], 0, v[2:3]
	v_lshlrev_b32_e32 v2, 2, v155
	v_and_or_b32 v171, v165, 32, v150
	v_or3_b32 v146, v145, v166, v170
	v_ashrrev_i32_e32 v145, 31, v144
	v_lshl_add_u64 v[148:149], s[38:39], 0, v[142:143]
	v_lshl_add_u64 v[150:151], v[140:141], 0, v[2:3]
	v_lshlrev_b32_e32 v2, 2, v152
	v_and_b32_e32 v153, 0x7c0, v8
	v_lshrrev_b32_e32 v147, 1, v147
	v_lshlrev_b64 v[144:145], 13, v[144:145]
	v_lshl_add_u64 v[148:149], v[148:149], 0, v[2:3]
	v_lshlrev_b32_e32 v2, 2, v154
	v_and_or_b32 v162, v162, 32, v147
	v_ashrrev_i32_e32 v147, 31, v146
	v_lshl_add_u64 v[156:157], s[38:39], 0, v[144:145]
	v_lshl_add_u64 v[158:159], v[148:149], 0, v[2:3]
	v_lshlrev_b32_e32 v2, 2, v153
	v_and_b32_e32 v160, 0x7c0, v0
	v_lshlrev_b64 v[146:147], 13, v[146:147]
	v_lshl_add_u64 v[156:157], v[156:157], 0, v[2:3]
	v_lshlrev_b32_e32 v2, 2, v162
	v_lshl_add_u64 v[164:165], s[38:39], 0, v[146:147]
	global_load_dwordx4 v[140:143], v[150:151], off nt
	global_load_dwordx4 v[144:147], v[150:151], off offset:16 nt
	v_lshl_add_u64 v[166:167], v[156:157], 0, v[2:3]
	v_lshlrev_b32_e32 v2, 2, v160
	global_load_dwordx4 v[148:151], v[158:159], off offset:16 nt
	global_load_dwordx4 v[152:155], v[158:159], off nt
	v_lshl_add_u64 v[164:165], v[164:165], 0, v[2:3]
	v_lshlrev_b32_e32 v2, 2, v171
	global_load_dwordx4 v[156:159], v[166:167], off nt
	global_load_dwordx4 v[160:163], v[166:167], off offset:16 nt
	v_lshl_add_u64 v[172:173], v[164:165], 0, v[2:3]
	global_load_dwordx4 v[164:167], v[172:173], off nt
	global_load_dwordx4 v[168:171], v[172:173], off offset:16 nt
	v_lshl_add_u64 v[172:173], v[4:5], 0, s[0:1]
	v_add_co_u32_e32 v174, vcc, s4, v172
	s_add_u32 s0, s0, 0x8000
	s_nop 0
	v_addc_co_u32_e32 v175, vcc, 0, v173, vcc
	v_add_co_u32_e32 v176, vcc, s5, v172
	s_addc_u32 s1, s1, 0
	s_nop 0
	v_addc_co_u32_e32 v177, vcc, 0, v173, vcc
	v_add_co_u32_e32 v178, vcc, s6, v172
	v_lshl_add_u64 v[0:1], v[0:1], 0, s[2:3]
	v_add_u32_e32 v7, 0x800, v7
	v_lshl_add_u64 v[8:9], v[8:9], 0, s[2:3]
	v_add_u32_e32 v11, 0x800, v11
	v_lshl_add_u64 v[12:13], v[12:13], 0, s[2:3]
	v_add_u32_e32 v15, 0x800, v15
	v_lshl_add_u64 v[16:17], v[16:17], 0, s[2:3]
	v_add_u32_e32 v19, 0x800, v19
	v_addc_co_u32_e32 v179, vcc, 0, v173, vcc
	s_waitcnt vmcnt(31)
	v_cvt_pk_f16_f32 v20, v20, v21
	v_cvt_pk_f16_f32 v21, v22, v23
	s_waitcnt vmcnt(30)
	v_cvt_pk_f16_f32 v22, v24, v25
	v_cvt_pk_f16_f32 v23, v26, v27
	global_store_dwordx4 v[52:53], v[20:23], off sc1
	s_waitcnt vmcnt(29)
	s_nop 0
	v_cvt_pk_f16_f32 v20, v32, v33
	v_cvt_pk_f16_f32 v21, v34, v35
	v_cvt_pk_f16_f32 v22, v28, v29
	v_cvt_pk_f16_f32 v23, v30, v31
	global_store_dwordx4 v[54:55], v[20:23], off sc1
	s_waitcnt vmcnt(29)
	s_nop 0
	v_cvt_pk_f16_f32 v20, v36, v37
	v_cvt_pk_f16_f32 v21, v38, v39
	s_waitcnt vmcnt(28)
	v_cvt_pk_f16_f32 v22, v40, v41
	v_cvt_pk_f16_f32 v23, v42, v43
	global_store_dwordx4 v[56:57], v[20:23], off sc1
	s_waitcnt vmcnt(28)
	s_nop 0
	v_cvt_pk_f16_f32 v20, v44, v45
	v_cvt_pk_f16_f32 v21, v46, v47
	s_waitcnt vmcnt(27)
	v_cvt_pk_f16_f32 v22, v48, v49
	v_cvt_pk_f16_f32 v23, v50, v51
	global_store_dwordx4 v[58:59], v[20:23], off sc1
	s_waitcnt vmcnt(27)
	v_cvt_pk_f16_f32 v60, v60, v61
	v_cvt_pk_f16_f32 v61, v62, v63
	s_waitcnt vmcnt(26)
	v_cvt_pk_f16_f32 v62, v64, v65
	v_cvt_pk_f16_f32 v63, v66, v67
	global_store_dwordx4 v[92:93], v[60:63], off sc1
	s_waitcnt vmcnt(25)
	s_nop 0
	v_cvt_pk_f16_f32 v60, v72, v73
	v_cvt_pk_f16_f32 v61, v74, v75
	v_cvt_pk_f16_f32 v62, v68, v69
	v_cvt_pk_f16_f32 v63, v70, v71
	global_store_dwordx4 v[94:95], v[60:63], off sc1
	s_waitcnt vmcnt(25)
	s_nop 0
	v_cvt_pk_f16_f32 v60, v76, v77
	v_cvt_pk_f16_f32 v61, v78, v79
	s_waitcnt vmcnt(24)
	v_cvt_pk_f16_f32 v62, v80, v81
	v_cvt_pk_f16_f32 v63, v82, v83
	global_store_dwordx4 v[96:97], v[60:63], off sc1
	s_waitcnt vmcnt(24)
	s_nop 0
	v_cvt_pk_f16_f32 v60, v84, v85
	v_cvt_pk_f16_f32 v61, v86, v87
	s_waitcnt vmcnt(23)
	v_cvt_pk_f16_f32 v62, v88, v89
	v_cvt_pk_f16_f32 v63, v90, v91
	global_store_dwordx4 v[98:99], v[60:63], off sc1
	s_waitcnt vmcnt(23)
	v_cvt_pk_f16_f32 v100, v100, v101
	v_cvt_pk_f16_f32 v101, v102, v103
	s_waitcnt vmcnt(22)
	v_cvt_pk_f16_f32 v102, v104, v105
	v_cvt_pk_f16_f32 v103, v106, v107
	global_store_dwordx4 v[132:133], v[100:103], off sc1
	s_waitcnt vmcnt(21)
	s_nop 0
	v_cvt_pk_f16_f32 v100, v112, v113
	v_cvt_pk_f16_f32 v101, v114, v115
	v_cvt_pk_f16_f32 v102, v108, v109
	v_cvt_pk_f16_f32 v103, v110, v111
	global_store_dwordx4 v[134:135], v[100:103], off sc1
	s_waitcnt vmcnt(21)
	s_nop 0
	v_cvt_pk_f16_f32 v100, v116, v117
	v_cvt_pk_f16_f32 v101, v118, v119
	s_waitcnt vmcnt(20)
	v_cvt_pk_f16_f32 v102, v120, v121
	v_cvt_pk_f16_f32 v103, v122, v123
	global_store_dwordx4 v[136:137], v[100:103], off sc1
	s_waitcnt vmcnt(20)
	s_nop 0
	v_cvt_pk_f16_f32 v100, v124, v125
	v_cvt_pk_f16_f32 v101, v126, v127
	s_waitcnt vmcnt(19)
	v_cvt_pk_f16_f32 v102, v128, v129
	v_cvt_pk_f16_f32 v103, v130, v131
	global_store_dwordx4 v[138:139], v[100:103], off sc1
	s_waitcnt vmcnt(19)
	v_cvt_pk_f16_f32 v140, v140, v141
	v_cvt_pk_f16_f32 v141, v142, v143
	s_waitcnt vmcnt(18)
	v_cvt_pk_f16_f32 v142, v144, v145
	v_cvt_pk_f16_f32 v143, v146, v147
	global_store_dwordx4 v[172:173], v[140:143], off sc1
	s_waitcnt vmcnt(17)
	s_nop 0
	v_cvt_pk_f16_f32 v140, v152, v153
	v_cvt_pk_f16_f32 v141, v154, v155
	v_cvt_pk_f16_f32 v142, v148, v149
	v_cvt_pk_f16_f32 v143, v150, v151
	global_store_dwordx4 v[174:175], v[140:143], off sc1
	s_waitcnt vmcnt(17)
	s_nop 0
	v_cvt_pk_f16_f32 v140, v156, v157
	v_cvt_pk_f16_f32 v141, v158, v159
	s_waitcnt vmcnt(16)
	v_cvt_pk_f16_f32 v142, v160, v161
	v_cvt_pk_f16_f32 v143, v162, v163
	global_store_dwordx4 v[176:177], v[140:143], off sc1
	s_waitcnt vmcnt(16)
	s_nop 0
	v_cvt_pk_f16_f32 v140, v164, v165
	v_cvt_pk_f16_f32 v141, v166, v167
	s_waitcnt vmcnt(15)
	v_cvt_pk_f16_f32 v142, v168, v169
	v_cvt_pk_f16_f32 v143, v170, v171
	global_store_dwordx4 v[178:179], v[140:143], off sc1
	s_sleep 127
